# phase D hyena transpose unit: 8 loads in flight then LDS scatter, 8 LDS row reads then stores (was load-wait-scatter x8)
# baseline (speedup 1.0000x reference)
; #define LAS __attribute__((address_space(3)))
; #define GAS __attribute__((address_space(1)))
; #define LDS_WAIT() asm volatile("s_waitcnt lgkmcnt(0)" ::: "memory")
; __device__ __forceinline__ void ph_hy_transpose(Frame& F, bool last) {
;     ...
;     for (int u = gw; u < ntt * 4; u += NGW) {
;         const int tt = u >> 2, cb = u & 3;
;         int b, s0, rowbase, posbase;
;         if (tt < 1024) { b = tt >> 6; s0 = (tt & 63) * 64; rowbase = b * SEQ; posbase = 0; }
;         else { const int t2 = tt - 1024; b = t2 >> 2; s0 = (t2 & 3) * 64; rowbase = NLAT + b * CTXL; posbase = SEQ; }
; #pragma unroll 2
;         for (int it = 0; it < 8; ++it) { const int c = rsub + 8 * it;
;             const u32x4 v = *(const GAS u32x4*)(HYO + ((size_t)(cb * 64 + c) * NB + b) * SPB + posbase + s0 + cseg * 8); const unsigned a[4] = {v.x, v.y, v.z, v.w};
; #pragma unroll
;             for (int e = 0; e < 4; ++e) { tile[(cseg * 8 + 2 * e) * 72 + c] = (bf16_t)(a[e] & 0xffffu); tile[(cseg * 8 + 2 * e + 1) * 72 + c] = (bf16_t)(a[e] >> 16); } }
;         LDS_WAIT(); asm volatile("" ::: "memory");
; #pragma unroll 2
;         for (int it = 0; it < 8; ++it) { const int p = rsub + 8 * it;
;             const u32x4 v = *(const LAS u32x4*)(tile + p * 72 + cseg * 8);
;             *(GAS u32x4*)((bf16_t*)(F.ws + WS_MIX) + (size_t)(rowbase + s0 + p) * DM + 768 + cb * 64 + cseg * 8) = v; }
;         LDS_WAIT(); asm volatile("" ::: "memory");
;     }
.LBB0_609:
	s_mul_hi_i32 s0, s18, 0x2200
	s_mulk_i32 s18, 0x2200
	s_lshl_b32 s19, s38, 1
	s_mov_b32 s37, s23
	s_add_u32 s21, s18, s19
	s_addc_u32 s0, s0, 0
	s_lshl_b64 s[18:19], s[36:37], 1
	s_add_u32 s18, s21, s18
	s_addc_u32 s19, s0, s19
	v_lshl_add_u64 v[4:5], v[0:1], 0, s[18:19]
	v_lshl_add_u64 v[6:7], v[2:3], 0, s[18:19]
	s_mov_b64 s[38:39], 0
	v_mov_b32_e32 v11, v9
	global_load_dwordx4 v[44:47], v[6:7], off
	global_load_dwordx4 v[48:51], v[4:5], off
	s_mov_b32 s38, 0x220000
	v_lshl_add_u64 v[80:81], v[6:7], 0, s[38:39]
	v_lshl_add_u64 v[82:83], v[4:5], 0, s[38:39]
	global_load_dwordx4 v[52:55], v[80:81], off
	global_load_dwordx4 v[56:59], v[82:83], off
	s_mov_b32 s38, 0x440000
	v_lshl_add_u64 v[84:85], v[6:7], 0, s[38:39]
	v_lshl_add_u64 v[86:87], v[4:5], 0, s[38:39]
	global_load_dwordx4 v[60:63], v[84:85], off
	global_load_dwordx4 v[64:67], v[86:87], off
	s_mov_b32 s38, 0x660000
	v_lshl_add_u64 v[88:89], v[6:7], 0, s[38:39]
	v_lshl_add_u64 v[90:91], v[4:5], 0, s[38:39]
	global_load_dwordx4 v[68:71], v[88:89], off
	global_load_dwordx4 v[72:75], v[90:91], off
	s_add_i32 s0, s5, s36
	v_add_u32_e32 v4, s0, v8
	v_ashrrev_i32_e32 v5, 31, v4
	v_lshlrev_b64 v[6:7], 11, v[4:5]
	v_lshl_add_u64 v[6:7], s[2:3], 0, v[6:7]
	v_lshl_add_u64 v[6:7], v[6:7], 0, s[22:23]
	v_lshl_add_u64 v[6:7], v[6:7], 0, v[192:193]
	v_add_co_u32_e32 v12, vcc, 0x36d00000, v6
	s_nop 1
	v_addc_co_u32_e32 v13, vcc, 0, v7, vcc
	s_mov_b32 s38, 0x4000
	v_lshl_add_u64 v[14:15], v[12:13], 0, s[38:39]
	v_lshl_add_u64 v[16:17], v[14:15], 0, s[38:39]
	v_lshl_add_u64 v[18:19], v[16:17], 0, s[38:39]
	v_lshl_add_u64 v[20:21], v[18:19], 0, s[38:39]
	v_lshl_add_u64 v[22:23], v[20:21], 0, s[38:39]
	v_lshl_add_u64 v[24:25], v[22:23], 0, s[38:39]
	v_lshl_add_u64 v[26:27], v[24:25], 0, s[38:39]
	s_waitcnt vmcnt(7)
	ds_write_b16 v9, v44
	ds_write_b16_d16_hi v9, v44 offset:144
	ds_write_b16 v9, v45 offset:288
	ds_write_b16_d16_hi v9, v45 offset:432
	ds_write_b16 v9, v46 offset:576
	ds_write_b16_d16_hi v9, v46 offset:720
	ds_write_b16 v9, v47 offset:864
	ds_write_b16_d16_hi v9, v47 offset:1008
	s_waitcnt vmcnt(6)
	ds_write_b16 v9, v48 offset:16
	ds_write_b16_d16_hi v9, v48 offset:160
	ds_write_b16 v9, v49 offset:304
	ds_write_b16_d16_hi v9, v49 offset:448
	ds_write_b16 v9, v50 offset:592
	ds_write_b16_d16_hi v9, v50 offset:736
	ds_write_b16 v9, v51 offset:880
	ds_write_b16_d16_hi v9, v51 offset:1024
	s_waitcnt vmcnt(5)
	ds_write_b16 v9, v52 offset:32
	ds_write_b16_d16_hi v9, v52 offset:176
	ds_write_b16 v9, v53 offset:320
	ds_write_b16_d16_hi v9, v53 offset:464
	ds_write_b16 v9, v54 offset:608
	ds_write_b16_d16_hi v9, v54 offset:752
	ds_write_b16 v9, v55 offset:896
	ds_write_b16_d16_hi v9, v55 offset:1040
	s_waitcnt vmcnt(4)
	ds_write_b16 v9, v56 offset:48
	ds_write_b16_d16_hi v9, v56 offset:192
	ds_write_b16 v9, v57 offset:336
	ds_write_b16_d16_hi v9, v57 offset:480
	ds_write_b16 v9, v58 offset:624
	ds_write_b16_d16_hi v9, v58 offset:768
	ds_write_b16 v9, v59 offset:912
	ds_write_b16_d16_hi v9, v59 offset:1056
	s_waitcnt vmcnt(3)
	ds_write_b16 v9, v60 offset:64
	ds_write_b16_d16_hi v9, v60 offset:208
	ds_write_b16 v9, v61 offset:352
	ds_write_b16_d16_hi v9, v61 offset:496
	ds_write_b16 v9, v62 offset:640
	ds_write_b16_d16_hi v9, v62 offset:784
	ds_write_b16 v9, v63 offset:928
	ds_write_b16_d16_hi v9, v63 offset:1072
	s_waitcnt vmcnt(2)
	ds_write_b16 v9, v64 offset:80
	ds_write_b16_d16_hi v9, v64 offset:224
	ds_write_b16 v9, v65 offset:368
	ds_write_b16_d16_hi v9, v65 offset:512
	ds_write_b16 v9, v66 offset:656
	ds_write_b16_d16_hi v9, v66 offset:800
	ds_write_b16 v9, v67 offset:944
	ds_write_b16_d16_hi v9, v67 offset:1088
	s_waitcnt vmcnt(1)
	ds_write_b16 v9, v68 offset:96
	ds_write_b16_d16_hi v9, v68 offset:240
	ds_write_b16 v9, v69 offset:384
	ds_write_b16_d16_hi v9, v69 offset:528
	ds_write_b16 v9, v70 offset:672
	ds_write_b16_d16_hi v9, v70 offset:816
	ds_write_b16 v9, v71 offset:960
	ds_write_b16_d16_hi v9, v71 offset:1104
	s_waitcnt vmcnt(0)
	ds_write_b16 v9, v72 offset:112
	ds_write_b16_d16_hi v9, v72 offset:256
	ds_write_b16 v9, v73 offset:400
	ds_write_b16_d16_hi v9, v73 offset:544
	ds_write_b16 v9, v74 offset:688
	ds_write_b16_d16_hi v9, v74 offset:832
	ds_write_b16 v9, v75 offset:976
	ds_write_b16_d16_hi v9, v75 offset:1120
	s_waitcnt lgkmcnt(0)
	ds_read_b128 v[92:95], v10
	ds_read_b128 v[96:99], v10 offset:1152
	ds_read_b128 v[100:103], v10 offset:2304
	ds_read_b128 v[104:107], v10 offset:3456
	ds_read_b128 v[108:111], v10 offset:4608
	ds_read_b128 v[112:115], v10 offset:5760
	ds_read_b128 v[116:119], v10 offset:6912
	ds_read_b128 v[120:123], v10 offset:8064
	s_waitcnt lgkmcnt(7)
	global_store_dwordx4 v[12:13], v[92:95], off offset:1536
	s_waitcnt lgkmcnt(6)
	global_store_dwordx4 v[14:15], v[96:99], off offset:1536
	s_waitcnt lgkmcnt(5)
	global_store_dwordx4 v[16:17], v[100:103], off offset:1536
	s_waitcnt lgkmcnt(4)
	global_store_dwordx4 v[18:19], v[104:107], off offset:1536
	s_waitcnt lgkmcnt(3)
	global_store_dwordx4 v[20:21], v[108:111], off offset:1536
	s_waitcnt lgkmcnt(2)
	global_store_dwordx4 v[22:23], v[112:115], off offset:1536
	s_waitcnt lgkmcnt(1)
	global_store_dwordx4 v[24:25], v[116:119], off offset:1536
	s_waitcnt lgkmcnt(0)
	global_store_dwordx4 v[26:27], v[120:123], off offset:1536
	s_movk_i32 s5, 0x2400
	s_waitcnt lgkmcnt(0)
	v_readlane_b32 s8, v255, 14
	s_add_i32 s4, s4, s8
	s_cmp_ge_i32 s4, s20
	v_readlane_b32 s9, v255, 15
	s_cbranch_scc0 .LBB0_605
